# v45 stack plus mLSTM chunk-output LDS tile fills pipelined (all loads in flight, counted waits)
# baseline (speedup 1.0000x reference)
; #define LAS __attribute__((address_space(3)))
; DI void ml3_unit(const Params& P, const Frame& F, int L, int cidx) {
;     ...
;     for (int id = F.tid; id < 3072; id += NTHR) { const int which = id >> 10, rem = id & 1023, row = rem >> 4, ch = rem & 15;
;         if (which == 0) *(LAS u32x4*)(Qs + row * 272 + ch * 16) = *(const u32x4*)(ZC + (r0 + row) * 2560 + 1536 + h * 128 + ch * 8);
;         else if (which == 1) *(LAS u32x4*)(Ks + row * 272 + ch * 16) = *(const u32x4*)(ZC + (r0 + row) * 2560 + 2048 + h * 128 + ch * 8);
;         else *(LAS u32x4*)(Vx + row * 304 + ch * 16) = *(const u32x4*)(Z + (r0 + row) * NZ + 6144 + h * 128 + ch * 8); }
.LBB0_1132:
	s_movk_i32 s66, 0x3ff
	v_bfe_u32 v154, v6, 4, 6
	v_cmp_lt_u32_e32 vcc, s66, v6
	s_and_saveexec_b64 s[66:67], vcc
	s_xor_b64 s[66:67], exec, s[66:67]
	s_cbranch_execz .Lm3a_0_1138
	v_and_b32_e32 v150, 0xfffffc00, v6
	s_movk_i32 s68, 0x400
	v_cmp_ne_u32_e32 vcc, s68, v150
	v_or_b32_e32 v157, s62, v154
	v_mov_b32_e32 v156, s63
	s_and_saveexec_b64 s[68:69], vcc
	s_xor_b64 s[68:69], exec, s[68:69]
	v_mov_b64_e32 v[150:151], s[34:35]
	v_mad_u64_u32 v[150:151], s[74:75], v157, s33, v[150:151]
	v_mov_b32_e32 v152, v151
	v_mad_u64_u32 v[152:153], s[74:75], v156, s33, v[152:153]
	v_mov_b32_e32 v151, v152
	s_mov_b64 s[74:75], 0x3000
	v_lshl_add_u64 v[150:151], v[150:151], 0, s[74:75]
	s_or_saveexec_b64 s[68:69], s[68:69]
	v_mov_b32_e32 v152, 0x130
	v_mov_b32_e32 v153, v69
	s_xor_b64 exec, exec, s[68:69]
	v_mov_b64_e32 v[150:151], s[36:37]
	v_mad_u64_u32 v[150:151], s[74:75], v157, s70, v[150:151]
	v_mov_b32_e32 v152, v151
	v_mad_u64_u32 v[152:153], s[74:75], v156, s70, v[152:153]
	v_mov_b32_e32 v151, v152
	s_mov_b64 s[74:75], 0x1000
	v_lshl_add_u64 v[150:151], v[150:151], 0, s[74:75]
	v_mov_b32_e32 v152, 0x110
	v_mov_b32_e32 v153, v70
	s_or_b64 exec, exec, s[68:69]
.Lm3a_0_1138:
	s_andn2_saveexec_b64 s[66:67], s[66:67]
	s_cbranch_execz .Lm3a_t0
	v_lshrrev_b32_e32 v150, 4, v6
	v_or_b32_e32 v152, s62, v150
	v_mov_b64_e32 v[150:151], s[36:37]
	s_mul_i32 s74, s63, 0x1400
	v_mad_u64_u32 v[150:151], s[68:69], v152, s70, v[150:151]
	v_add_u32_e32 v151, s74, v151
	s_mov_b64 s[68:69], 0xc00
	v_lshl_add_u64 v[150:151], v[150:151], 0, s[68:69]
	v_mov_b32_e32 v152, 0x110
	v_mov_b32_e32 v153, v52
	s_branch .Lm3a_t0
.Lm3a_t0:
	s_or_b64 exec, exec, s[66:67]
	v_lshl_add_u64 v[150:151], v[150:151], 0, s[0:1]
	v_lshl_add_u64 v[150:151], v[150:151], 0, v[50:51]
	global_load_dwordx4 v[156:159], v[150:151], off
	v_mad_u32_u24 v150, v152, v154, v153
	v_add_u32_e32 v6, 0x200, v6
	s_movk_i32 s66, 0x3ff
	v_bfe_u32 v170, v6, 4, 6
	v_cmp_lt_u32_e32 vcc, s66, v6
	s_and_saveexec_b64 s[66:67], vcc
	s_xor_b64 s[66:67], exec, s[66:67]
	s_cbranch_execz .Lm3a_1_1138
	v_and_b32_e32 v166, 0xfffffc00, v6
	s_movk_i32 s68, 0x400
	v_cmp_ne_u32_e32 vcc, s68, v166
	v_or_b32_e32 v173, s62, v170
	v_mov_b32_e32 v172, s63
	s_and_saveexec_b64 s[68:69], vcc
	s_xor_b64 s[68:69], exec, s[68:69]
	v_mov_b64_e32 v[166:167], s[34:35]
	v_mad_u64_u32 v[166:167], s[74:75], v173, s33, v[166:167]
	v_mov_b32_e32 v168, v167
	v_mad_u64_u32 v[168:169], s[74:75], v172, s33, v[168:169]
	v_mov_b32_e32 v167, v168
	s_mov_b64 s[74:75], 0x3000
	v_lshl_add_u64 v[166:167], v[166:167], 0, s[74:75]
	s_or_saveexec_b64 s[68:69], s[68:69]
	v_mov_b32_e32 v168, 0x130
	v_mov_b32_e32 v169, v69
	s_xor_b64 exec, exec, s[68:69]
	v_mov_b64_e32 v[166:167], s[36:37]
	v_mad_u64_u32 v[166:167], s[74:75], v173, s70, v[166:167]
	v_mov_b32_e32 v168, v167
	v_mad_u64_u32 v[168:169], s[74:75], v172, s70, v[168:169]
	v_mov_b32_e32 v167, v168
	s_mov_b64 s[74:75], 0x1000
	v_lshl_add_u64 v[166:167], v[166:167], 0, s[74:75]
	v_mov_b32_e32 v168, 0x110
	v_mov_b32_e32 v169, v70
	s_or_b64 exec, exec, s[68:69]
.Lm3a_1_1138:
	s_andn2_saveexec_b64 s[66:67], s[66:67]
	s_cbranch_execz .Lm3a_t1
	v_lshrrev_b32_e32 v166, 4, v6
	v_or_b32_e32 v168, s62, v166
	v_mov_b64_e32 v[166:167], s[36:37]
	s_mul_i32 s74, s63, 0x1400
	v_mad_u64_u32 v[166:167], s[68:69], v168, s70, v[166:167]
	v_add_u32_e32 v167, s74, v167
	s_mov_b64 s[68:69], 0xc00
	v_lshl_add_u64 v[166:167], v[166:167], 0, s[68:69]
	v_mov_b32_e32 v168, 0x110
	v_mov_b32_e32 v169, v52
	s_branch .Lm3a_t1
.Lm3a_t1:
	s_or_b64 exec, exec, s[66:67]
	v_lshl_add_u64 v[166:167], v[166:167], 0, s[0:1]
	v_lshl_add_u64 v[166:167], v[166:167], 0, v[50:51]
	global_load_dwordx4 v[172:175], v[166:167], off
	v_mad_u32_u24 v166, v168, v170, v169
	v_add_u32_e32 v6, 0x200, v6
	s_movk_i32 s66, 0x3ff
	v_bfe_u32 v186, v6, 4, 6
	v_cmp_lt_u32_e32 vcc, s66, v6
	s_and_saveexec_b64 s[66:67], vcc
	s_xor_b64 s[66:67], exec, s[66:67]
	s_cbranch_execz .Lm3a_2_1138
	v_and_b32_e32 v182, 0xfffffc00, v6
	s_movk_i32 s68, 0x400
	v_cmp_ne_u32_e32 vcc, s68, v182
	v_or_b32_e32 v189, s62, v186
	v_mov_b32_e32 v188, s63
	s_and_saveexec_b64 s[68:69], vcc
	s_xor_b64 s[68:69], exec, s[68:69]
	v_mov_b64_e32 v[182:183], s[34:35]
	v_mad_u64_u32 v[182:183], s[74:75], v189, s33, v[182:183]
	v_mov_b32_e32 v184, v183
	v_mad_u64_u32 v[184:185], s[74:75], v188, s33, v[184:185]
	v_mov_b32_e32 v183, v184
	s_mov_b64 s[74:75], 0x3000
	v_lshl_add_u64 v[182:183], v[182:183], 0, s[74:75]
	s_or_saveexec_b64 s[68:69], s[68:69]
	v_mov_b32_e32 v184, 0x130
	v_mov_b32_e32 v185, v69
	s_xor_b64 exec, exec, s[68:69]
	v_mov_b64_e32 v[182:183], s[36:37]
	v_mad_u64_u32 v[182:183], s[74:75], v189, s70, v[182:183]
	v_mov_b32_e32 v184, v183
	v_mad_u64_u32 v[184:185], s[74:75], v188, s70, v[184:185]
	v_mov_b32_e32 v183, v184
	s_mov_b64 s[74:75], 0x1000
	v_lshl_add_u64 v[182:183], v[182:183], 0, s[74:75]
	v_mov_b32_e32 v184, 0x110
	v_mov_b32_e32 v185, v70
	s_or_b64 exec, exec, s[68:69]
.Lm3a_2_1138:
	s_andn2_saveexec_b64 s[66:67], s[66:67]
	s_cbranch_execz .Lm3a_t2
	v_lshrrev_b32_e32 v182, 4, v6
	v_or_b32_e32 v184, s62, v182
	v_mov_b64_e32 v[182:183], s[36:37]
	s_mul_i32 s74, s63, 0x1400
	v_mad_u64_u32 v[182:183], s[68:69], v184, s70, v[182:183]
	v_add_u32_e32 v183, s74, v183
	s_mov_b64 s[68:69], 0xc00
	v_lshl_add_u64 v[182:183], v[182:183], 0, s[68:69]
	v_mov_b32_e32 v184, 0x110
	v_mov_b32_e32 v185, v52
	s_branch .Lm3a_t2
; #define LAS __attribute__((address_space(3)))
; DI void ml3_unit(const Params& P, const Frame& F, int L, int cidx) {
;     ...
;     for (int id = F.tid; id < 3072; id += NTHR) { const int which = id >> 10, rem = id & 1023, row = rem >> 4, ch = rem & 15;
;         if (which == 0) *(LAS u32x4*)(Qs + row * 272 + ch * 16) = *(const u32x4*)(ZC + (r0 + row) * 2560 + 1536 + h * 128 + ch * 8);
;         else if (which == 1) *(LAS u32x4*)(Ks + row * 272 + ch * 16) = *(const u32x4*)(ZC + (r0 + row) * 2560 + 2048 + h * 128 + ch * 8);
;         else *(LAS u32x4*)(Vx + row * 304 + ch * 16) = *(const u32x4*)(Z + (r0 + row) * NZ + 6144 + h * 128 + ch * 8); }
.Lm3a_t2:
	s_or_b64 exec, exec, s[66:67]
	v_lshl_add_u64 v[182:183], v[182:183], 0, s[0:1]
	v_lshl_add_u64 v[182:183], v[182:183], 0, v[50:51]
	global_load_dwordx4 v[188:191], v[182:183], off
	v_mad_u32_u24 v182, v184, v186, v185
	v_add_u32_e32 v6, 0x200, v6
	s_movk_i32 s66, 0x3ff
	v_bfe_u32 v202, v6, 4, 6
	v_cmp_lt_u32_e32 vcc, s66, v6
	s_and_saveexec_b64 s[66:67], vcc
	s_xor_b64 s[66:67], exec, s[66:67]
	s_cbranch_execz .Lm3a_3_1138
	v_and_b32_e32 v198, 0xfffffc00, v6
	s_movk_i32 s68, 0x400
	v_cmp_ne_u32_e32 vcc, s68, v198
	v_or_b32_e32 v205, s62, v202
	v_mov_b32_e32 v204, s63
	s_and_saveexec_b64 s[68:69], vcc
	s_xor_b64 s[68:69], exec, s[68:69]
	v_mov_b64_e32 v[198:199], s[34:35]
	v_mad_u64_u32 v[198:199], s[74:75], v205, s33, v[198:199]
	v_mov_b32_e32 v200, v199
	v_mad_u64_u32 v[200:201], s[74:75], v204, s33, v[200:201]
	v_mov_b32_e32 v199, v200
	s_mov_b64 s[74:75], 0x3000
	v_lshl_add_u64 v[198:199], v[198:199], 0, s[74:75]
	s_or_saveexec_b64 s[68:69], s[68:69]
	v_mov_b32_e32 v200, 0x130
	v_mov_b32_e32 v201, v69
	s_xor_b64 exec, exec, s[68:69]
	v_mov_b64_e32 v[198:199], s[36:37]
	v_mad_u64_u32 v[198:199], s[74:75], v205, s70, v[198:199]
	v_mov_b32_e32 v200, v199
	v_mad_u64_u32 v[200:201], s[74:75], v204, s70, v[200:201]
	v_mov_b32_e32 v199, v200
	s_mov_b64 s[74:75], 0x1000
	v_lshl_add_u64 v[198:199], v[198:199], 0, s[74:75]
	v_mov_b32_e32 v200, 0x110
	v_mov_b32_e32 v201, v70
	s_or_b64 exec, exec, s[68:69]
.Lm3a_3_1138:
	s_andn2_saveexec_b64 s[66:67], s[66:67]
	s_cbranch_execz .Lm3a_t3
	v_lshrrev_b32_e32 v198, 4, v6
	v_or_b32_e32 v200, s62, v198
	v_mov_b64_e32 v[198:199], s[36:37]
	s_mul_i32 s74, s63, 0x1400
	v_mad_u64_u32 v[198:199], s[68:69], v200, s70, v[198:199]
	v_add_u32_e32 v199, s74, v199
	s_mov_b64 s[68:69], 0xc00
	v_lshl_add_u64 v[198:199], v[198:199], 0, s[68:69]
	v_mov_b32_e32 v200, 0x110
	v_mov_b32_e32 v201, v52
	s_branch .Lm3a_t3
.Lm3a_t3:
	s_or_b64 exec, exec, s[66:67]
	v_lshl_add_u64 v[198:199], v[198:199], 0, s[0:1]
	v_lshl_add_u64 v[198:199], v[198:199], 0, v[50:51]
	global_load_dwordx4 v[204:207], v[198:199], off
	v_mad_u32_u24 v198, v200, v202, v201
	v_add_u32_e32 v6, 0x200, v6
	s_movk_i32 s66, 0x3ff
	v_bfe_u32 v218, v6, 4, 6
	v_cmp_lt_u32_e32 vcc, s66, v6
	s_and_saveexec_b64 s[66:67], vcc
	s_xor_b64 s[66:67], exec, s[66:67]
	s_cbranch_execz .Lm3a_4_1138
	v_and_b32_e32 v214, 0xfffffc00, v6
	s_movk_i32 s68, 0x400
	v_cmp_ne_u32_e32 vcc, s68, v214
	v_or_b32_e32 v221, s62, v218
	v_mov_b32_e32 v220, s63
	s_and_saveexec_b64 s[68:69], vcc
	s_xor_b64 s[68:69], exec, s[68:69]
	v_mov_b64_e32 v[214:215], s[34:35]
	v_mad_u64_u32 v[214:215], s[74:75], v221, s33, v[214:215]
	v_mov_b32_e32 v216, v215
	v_mad_u64_u32 v[216:217], s[74:75], v220, s33, v[216:217]
	v_mov_b32_e32 v215, v216
	s_mov_b64 s[74:75], 0x3000
	v_lshl_add_u64 v[214:215], v[214:215], 0, s[74:75]
	s_or_saveexec_b64 s[68:69], s[68:69]
	v_mov_b32_e32 v216, 0x130
	v_mov_b32_e32 v217, v69
	s_xor_b64 exec, exec, s[68:69]
	v_mov_b64_e32 v[214:215], s[36:37]
	v_mad_u64_u32 v[214:215], s[74:75], v221, s70, v[214:215]
	v_mov_b32_e32 v216, v215
	v_mad_u64_u32 v[216:217], s[74:75], v220, s70, v[216:217]
	v_mov_b32_e32 v215, v216
	s_mov_b64 s[74:75], 0x1000
	v_lshl_add_u64 v[214:215], v[214:215], 0, s[74:75]
	v_mov_b32_e32 v216, 0x110
	v_mov_b32_e32 v217, v70
	s_or_b64 exec, exec, s[68:69]
.Lm3a_4_1138:
	s_andn2_saveexec_b64 s[66:67], s[66:67]
	s_cbranch_execz .Lm3a_t4
	v_lshrrev_b32_e32 v214, 4, v6
	v_or_b32_e32 v216, s62, v214
	v_mov_b64_e32 v[214:215], s[36:37]
	s_mul_i32 s74, s63, 0x1400
	v_mad_u64_u32 v[214:215], s[68:69], v216, s70, v[214:215]
	v_add_u32_e32 v215, s74, v215
	s_mov_b64 s[68:69], 0xc00
	v_lshl_add_u64 v[214:215], v[214:215], 0, s[68:69]
	v_mov_b32_e32 v216, 0x110
	v_mov_b32_e32 v217, v52
	s_branch .Lm3a_t4
.Lm3a_t4:
	s_or_b64 exec, exec, s[66:67]
	v_lshl_add_u64 v[214:215], v[214:215], 0, s[0:1]
	v_lshl_add_u64 v[214:215], v[214:215], 0, v[50:51]
	global_load_dwordx4 v[220:223], v[214:215], off
	v_mad_u32_u24 v214, v216, v218, v217
	v_add_u32_e32 v6, 0x200, v6
	s_movk_i32 s66, 0x3ff
	v_bfe_u32 v234, v6, 4, 6
	v_cmp_lt_u32_e32 vcc, s66, v6
	s_and_saveexec_b64 s[66:67], vcc
	s_xor_b64 s[66:67], exec, s[66:67]
	s_cbranch_execz .Lm3a_5_1138
	v_and_b32_e32 v230, 0xfffffc00, v6
	s_movk_i32 s68, 0x400
	v_cmp_ne_u32_e32 vcc, s68, v230
	v_or_b32_e32 v237, s62, v234
	v_mov_b32_e32 v236, s63
	s_and_saveexec_b64 s[68:69], vcc
	s_xor_b64 s[68:69], exec, s[68:69]
	v_mov_b64_e32 v[230:231], s[34:35]
	v_mad_u64_u32 v[230:231], s[74:75], v237, s33, v[230:231]
	v_mov_b32_e32 v232, v231
	v_mad_u64_u32 v[232:233], s[74:75], v236, s33, v[232:233]
	v_mov_b32_e32 v231, v232
	s_mov_b64 s[74:75], 0x3000
	v_lshl_add_u64 v[230:231], v[230:231], 0, s[74:75]
	s_or_saveexec_b64 s[68:69], s[68:69]
	v_mov_b32_e32 v232, 0x130
	v_mov_b32_e32 v233, v69
	s_xor_b64 exec, exec, s[68:69]
	v_mov_b64_e32 v[230:231], s[36:37]
	v_mad_u64_u32 v[230:231], s[74:75], v237, s70, v[230:231]
	v_mov_b32_e32 v232, v231
	v_mad_u64_u32 v[232:233], s[74:75], v236, s70, v[232:233]
	v_mov_b32_e32 v231, v232
	s_mov_b64 s[74:75], 0x1000
	v_lshl_add_u64 v[230:231], v[230:231], 0, s[74:75]
	v_mov_b32_e32 v232, 0x110
	v_mov_b32_e32 v233, v70
	s_or_b64 exec, exec, s[68:69]
.Lm3a_5_1138:
	s_andn2_saveexec_b64 s[66:67], s[66:67]
	s_cbranch_execz .Lm3a_t5
	v_lshrrev_b32_e32 v230, 4, v6
	v_or_b32_e32 v232, s62, v230
	v_mov_b64_e32 v[230:231], s[36:37]
	s_mul_i32 s74, s63, 0x1400
	v_mad_u64_u32 v[230:231], s[68:69], v232, s70, v[230:231]
	v_add_u32_e32 v231, s74, v231
	s_mov_b64 s[68:69], 0xc00
	v_lshl_add_u64 v[230:231], v[230:231], 0, s[68:69]
	v_mov_b32_e32 v232, 0x110
	v_mov_b32_e32 v233, v52
	s_branch .Lm3a_t5
.Lm3a_t5:
	s_or_b64 exec, exec, s[66:67]
	v_lshl_add_u64 v[230:231], v[230:231], 0, s[0:1]
	v_lshl_add_u64 v[230:231], v[230:231], 0, v[50:51]
	global_load_dwordx4 v[236:239], v[230:231], off
	v_mad_u32_u24 v230, v232, v234, v233
	s_waitcnt vmcnt(5)
	ds_write_b128 v150, v[156:159]
	s_waitcnt vmcnt(4)
	ds_write_b128 v166, v[172:175]
	s_waitcnt vmcnt(3)
	ds_write_b128 v182, v[188:191]
	s_waitcnt vmcnt(2)
	ds_write_b128 v198, v[204:207]
	s_waitcnt vmcnt(1)
	ds_write_b128 v214, v[220:223]
	s_waitcnt vmcnt(0)
	ds_write_b128 v230, v[236:239]

; #define LAS __attribute__((address_space(3)))
; DI void ml3_unit(const Params& P, const Frame& F, int L, int cidx) {
;     ...
;     for (int id = F.tid; id < 2304; id += NTHR) { const int row = id >> 4, ch = id & 15; *(LAS u32x4*)(Cs + row * 272 + ch * 16) = *(const u32x4*)(CST + row * 128 + ch * 8); }
.LBB0_1144:
	v_add_u32_e32 v222, 0x800, v6
	s_movk_i32 s0, 0x8ff
	v_cmp_ge_i32_e32 vcc, s0, v222
	s_mov_b64 s[64:65], exec
	s_and_b64 exec, exec, vcc
	v_ashrrev_i32_e32 v214, 4, v222
	v_lshlrev_b32_e32 v216, 7, v214
	v_ashrrev_i32_e32 v217, 31, v216
	v_lshl_add_u64 v[216:217], v[216:217], 1, v[4:5]
	v_mad_u64_u32 v[220:221], s[66:67], v214, s3, v[52:53]
	global_load_dwordx4 v[216:219], v[216:217], off
	s_mov_b64 exec, s[64:65]
	v_ashrrev_i32_e32 v150, 4, v6
	v_lshlrev_b32_e32 v152, 7, v150
	v_ashrrev_i32_e32 v153, 31, v152
	v_lshl_add_u64 v[152:153], v[152:153], 1, v[4:5]
	v_mad_u64_u32 v[156:157], s[66:67], v150, s3, v[52:53]
	global_load_dwordx4 v[152:155], v[152:153], off
	v_add_u32_e32 v6, 0x200, v6
	v_ashrrev_i32_e32 v166, 4, v6
	v_lshlrev_b32_e32 v168, 7, v166
	v_ashrrev_i32_e32 v169, 31, v168
	v_lshl_add_u64 v[168:169], v[168:169], 1, v[4:5]
	v_mad_u64_u32 v[172:173], s[66:67], v166, s3, v[52:53]
	global_load_dwordx4 v[168:171], v[168:169], off
	v_add_u32_e32 v6, 0x200, v6
	v_ashrrev_i32_e32 v182, 4, v6
	v_lshlrev_b32_e32 v184, 7, v182
	v_ashrrev_i32_e32 v185, 31, v184
	v_lshl_add_u64 v[184:185], v[184:185], 1, v[4:5]
	v_mad_u64_u32 v[188:189], s[66:67], v182, s3, v[52:53]
	global_load_dwordx4 v[184:187], v[184:185], off
	v_add_u32_e32 v6, 0x200, v6
	v_ashrrev_i32_e32 v198, 4, v6
	v_lshlrev_b32_e32 v200, 7, v198
	v_ashrrev_i32_e32 v201, 31, v200
	v_lshl_add_u64 v[200:201], v[200:201], 1, v[4:5]
	v_mad_u64_u32 v[204:205], s[66:67], v198, s3, v[52:53]
	global_load_dwordx4 v[200:203], v[200:201], off
	s_waitcnt vmcnt(3)
	ds_write_b128 v156, v[152:155] offset:54272
	s_waitcnt vmcnt(2)
	ds_write_b128 v172, v[168:171] offset:54272
	s_waitcnt vmcnt(1)
	ds_write_b128 v188, v[184:187] offset:54272
	s_waitcnt vmcnt(0)
	ds_write_b128 v204, v[200:203] offset:54272
	v_cmp_ge_i32_e32 vcc, s0, v222
	s_mov_b64 s[64:65], exec
	s_and_b64 exec, exec, vcc
	s_waitcnt vmcnt(0)
	ds_write_b128 v220, v[216:219] offset:54272
	s_mov_b64 exec, s[64:65]

.LBB0_1215:
	global_load_dword v1, v0, s[10:11] sc1
	s_waitcnt vmcnt(0)
	v_cmp_eq_u32_e32 vcc, 0, v1
	s_cbranch_vccnz .LBB0_1217
	s_mov_b64 s[18:19], -1
	s_mov_b64 s[22:23], -1
	s_branch .LBB0_1211
.LBB0_1217:
	s_cmp_lt_u32 s3, 0x40001
	s_mov_b64 s[18:19], 0
	s_cselect_b64 s[20:21], -1, 0
	s_mov_b64 s[22:23], -1
	s_and_b64 vcc, exec, s[20:21]
	s_cbranch_vccnz .LBB0_1214
	s_branch .LBB0_1211
	s_nop 0
	s_nop 0
	s_nop 0
	s_nop 0
	s_nop 0
	s_nop 0
	s_nop 0
	s_nop 0
	s_nop 0
.LBB0_1218:
	s_or_b64 exec, exec, s[14:15]
	s_and_b64 s[14:15], s[16:17], exec

; #define LAS __attribute__((address_space(3)))
; DI void ml3_unit(const Params& P, const Frame& F, int L, int cidx) {
;     ...
;     for (int id = F.tid; id < 3072; id += NTHR) { const int which = id >> 10, rem = id & 1023, row = rem >> 4, ch = rem & 15;
;         if (which == 0) *(LAS u32x4*)(Qs + row * 272 + ch * 16) = *(const u32x4*)(ZC + (r0 + row) * 2560 + 1536 + h * 128 + ch * 8);
;         else if (which == 1) *(LAS u32x4*)(Ks + row * 272 + ch * 16) = *(const u32x4*)(ZC + (r0 + row) * 2560 + 2048 + h * 128 + ch * 8);
;         else *(LAS u32x4*)(Vx + row * 304 + ch * 16) = *(const u32x4*)(Z + (r0 + row) * NZ + 6144 + h * 128 + ch * 8); }
.LBB0_2697:
	s_movk_i32 s68, 0x3ff
	v_bfe_u32 v154, v6, 4, 6
	v_cmp_lt_u32_e32 vcc, s68, v6
	s_and_saveexec_b64 s[68:69], vcc
	s_xor_b64 s[68:69], exec, s[68:69]
	s_cbranch_execz .Lm3b_0_2703
	v_and_b32_e32 v150, 0xfffffc00, v6
	s_movk_i32 s70, 0x400
	v_cmp_ne_u32_e32 vcc, s70, v150
	v_or_b32_e32 v157, s64, v154
	v_mov_b32_e32 v156, s65
	s_and_saveexec_b64 s[70:71], vcc
	s_xor_b64 s[70:71], exec, s[70:71]
	v_mov_b64_e32 v[150:151], s[34:35]
	v_mad_u64_u32 v[150:151], s[80:81], v157, s33, v[150:151]
	v_mov_b32_e32 v152, v151
	v_mad_u64_u32 v[152:153], s[80:81], v156, s33, v[152:153]
	v_mov_b32_e32 v151, v152
	s_mov_b64 s[80:81], 0x3000
	v_lshl_add_u64 v[150:151], v[150:151], 0, s[80:81]
	s_or_saveexec_b64 s[70:71], s[70:71]
	v_mov_b32_e32 v152, 0x130
	v_mov_b32_e32 v153, v69
	s_xor_b64 exec, exec, s[70:71]
	v_mov_b64_e32 v[150:151], s[36:37]
	v_mad_u64_u32 v[150:151], s[80:81], v157, s72, v[150:151]
	v_mov_b32_e32 v152, v151
	v_mad_u64_u32 v[152:153], s[80:81], v156, s72, v[152:153]
	v_mov_b32_e32 v151, v152
	v_lshl_add_u64 v[150:151], v[150:151], 0, s[56:57]
	v_mov_b32_e32 v152, 0x110
	v_mov_b32_e32 v153, v70
	s_or_b64 exec, exec, s[70:71]
.Lm3b_0_2703:
	s_andn2_saveexec_b64 s[68:69], s[68:69]
	s_cbranch_execz .Lm3b_t0
	v_lshrrev_b32_e32 v150, 4, v6
	v_or_b32_e32 v152, s64, v150
	v_mov_b64_e32 v[150:151], s[36:37]
	s_mul_i32 s80, s65, 0x1400
	v_mad_u64_u32 v[150:151], s[70:71], v152, s72, v[150:151]
	v_add_u32_e32 v151, s80, v151
	v_lshl_add_u64 v[150:151], v[150:151], 0, s[58:59]
	v_mov_b32_e32 v152, 0x110
	v_mov_b32_e32 v153, v52
	s_branch .Lm3b_t0
.Lm3b_t0:
	s_or_b64 exec, exec, s[68:69]
	v_lshl_add_u64 v[150:151], v[150:151], 0, s[0:1]
	v_lshl_add_u64 v[150:151], v[150:151], 0, v[50:51]
	global_load_dwordx4 v[156:159], v[150:151], off
	v_mad_u32_u24 v150, v152, v154, v153
	v_add_u32_e32 v6, 0x200, v6
	s_movk_i32 s68, 0x3ff
	v_bfe_u32 v170, v6, 4, 6
	v_cmp_lt_u32_e32 vcc, s68, v6
	s_and_saveexec_b64 s[68:69], vcc
	s_xor_b64 s[68:69], exec, s[68:69]
	s_cbranch_execz .Lm3b_1_2703
	v_and_b32_e32 v166, 0xfffffc00, v6
	s_movk_i32 s70, 0x400
	v_cmp_ne_u32_e32 vcc, s70, v166
	v_or_b32_e32 v173, s64, v170
	v_mov_b32_e32 v172, s65
	s_and_saveexec_b64 s[70:71], vcc
	s_xor_b64 s[70:71], exec, s[70:71]
	v_mov_b64_e32 v[166:167], s[34:35]
	v_mad_u64_u32 v[166:167], s[80:81], v173, s33, v[166:167]
	v_mov_b32_e32 v168, v167
	v_mad_u64_u32 v[168:169], s[80:81], v172, s33, v[168:169]
	v_mov_b32_e32 v167, v168
	s_mov_b64 s[80:81], 0x3000
	v_lshl_add_u64 v[166:167], v[166:167], 0, s[80:81]
	s_or_saveexec_b64 s[70:71], s[70:71]
	v_mov_b32_e32 v168, 0x130
	v_mov_b32_e32 v169, v69
	s_xor_b64 exec, exec, s[70:71]
	v_mov_b64_e32 v[166:167], s[36:37]
	v_mad_u64_u32 v[166:167], s[80:81], v173, s72, v[166:167]
	v_mov_b32_e32 v168, v167
	v_mad_u64_u32 v[168:169], s[80:81], v172, s72, v[168:169]
	v_mov_b32_e32 v167, v168
	v_lshl_add_u64 v[166:167], v[166:167], 0, s[56:57]
	v_mov_b32_e32 v168, 0x110
	v_mov_b32_e32 v169, v70
	s_or_b64 exec, exec, s[70:71]
.Lm3b_1_2703:
	s_andn2_saveexec_b64 s[68:69], s[68:69]
	s_cbranch_execz .Lm3b_t1
	v_lshrrev_b32_e32 v166, 4, v6
	v_or_b32_e32 v168, s64, v166
	v_mov_b64_e32 v[166:167], s[36:37]
	s_mul_i32 s80, s65, 0x1400
	v_mad_u64_u32 v[166:167], s[70:71], v168, s72, v[166:167]
	v_add_u32_e32 v167, s80, v167
	v_lshl_add_u64 v[166:167], v[166:167], 0, s[58:59]
	v_mov_b32_e32 v168, 0x110
	v_mov_b32_e32 v169, v52
	s_branch .Lm3b_t1
.Lm3b_t1:
	s_or_b64 exec, exec, s[68:69]
	v_lshl_add_u64 v[166:167], v[166:167], 0, s[0:1]
	v_lshl_add_u64 v[166:167], v[166:167], 0, v[50:51]
	global_load_dwordx4 v[172:175], v[166:167], off
	v_mad_u32_u24 v166, v168, v170, v169
	v_add_u32_e32 v6, 0x200, v6
	s_movk_i32 s68, 0x3ff
	v_bfe_u32 v186, v6, 4, 6
	v_cmp_lt_u32_e32 vcc, s68, v6
	s_and_saveexec_b64 s[68:69], vcc
	s_xor_b64 s[68:69], exec, s[68:69]
	s_cbranch_execz .Lm3b_2_2703
	v_and_b32_e32 v182, 0xfffffc00, v6
	s_movk_i32 s70, 0x400
	v_cmp_ne_u32_e32 vcc, s70, v182
	v_or_b32_e32 v189, s64, v186
	v_mov_b32_e32 v188, s65
	s_and_saveexec_b64 s[70:71], vcc
	s_xor_b64 s[70:71], exec, s[70:71]
	v_mov_b64_e32 v[182:183], s[34:35]
	v_mad_u64_u32 v[182:183], s[80:81], v189, s33, v[182:183]
	v_mov_b32_e32 v184, v183
	v_mad_u64_u32 v[184:185], s[80:81], v188, s33, v[184:185]
	v_mov_b32_e32 v183, v184
	s_mov_b64 s[80:81], 0x3000
	v_lshl_add_u64 v[182:183], v[182:183], 0, s[80:81]
	s_or_saveexec_b64 s[70:71], s[70:71]
	v_mov_b32_e32 v184, 0x130
	v_mov_b32_e32 v185, v69
	s_xor_b64 exec, exec, s[70:71]
	v_mov_b64_e32 v[182:183], s[36:37]
	v_mad_u64_u32 v[182:183], s[80:81], v189, s72, v[182:183]
	v_mov_b32_e32 v184, v183
	v_mad_u64_u32 v[184:185], s[80:81], v188, s72, v[184:185]
	v_mov_b32_e32 v183, v184
	v_lshl_add_u64 v[182:183], v[182:183], 0, s[56:57]
	v_mov_b32_e32 v184, 0x110
	v_mov_b32_e32 v185, v70
	s_or_b64 exec, exec, s[70:71]
.Lm3b_2_2703:
	s_andn2_saveexec_b64 s[68:69], s[68:69]
	s_cbranch_execz .Lm3b_t2
	v_lshrrev_b32_e32 v182, 4, v6
	v_or_b32_e32 v184, s64, v182
	v_mov_b64_e32 v[182:183], s[36:37]
	s_mul_i32 s80, s65, 0x1400
	v_mad_u64_u32 v[182:183], s[70:71], v184, s72, v[182:183]
	v_add_u32_e32 v183, s80, v183
	v_lshl_add_u64 v[182:183], v[182:183], 0, s[58:59]
	v_mov_b32_e32 v184, 0x110
	v_mov_b32_e32 v185, v52
	s_branch .Lm3b_t2
; #define LAS __attribute__((address_space(3)))
; DI void ml3_unit(const Params& P, const Frame& F, int L, int cidx) {
;     ...
;     for (int id = F.tid; id < 3072; id += NTHR) { const int which = id >> 10, rem = id & 1023, row = rem >> 4, ch = rem & 15;
;         if (which == 0) *(LAS u32x4*)(Qs + row * 272 + ch * 16) = *(const u32x4*)(ZC + (r0 + row) * 2560 + 1536 + h * 128 + ch * 8);
;         else if (which == 1) *(LAS u32x4*)(Ks + row * 272 + ch * 16) = *(const u32x4*)(ZC + (r0 + row) * 2560 + 2048 + h * 128 + ch * 8);
;         else *(LAS u32x4*)(Vx + row * 304 + ch * 16) = *(const u32x4*)(Z + (r0 + row) * NZ + 6144 + h * 128 + ch * 8); }
.Lm3b_t2:
	s_or_b64 exec, exec, s[68:69]
	v_lshl_add_u64 v[182:183], v[182:183], 0, s[0:1]
	v_lshl_add_u64 v[182:183], v[182:183], 0, v[50:51]
	global_load_dwordx4 v[188:191], v[182:183], off
	v_mad_u32_u24 v182, v184, v186, v185
	v_add_u32_e32 v6, 0x200, v6
	s_movk_i32 s68, 0x3ff
	v_bfe_u32 v202, v6, 4, 6
	v_cmp_lt_u32_e32 vcc, s68, v6
	s_and_saveexec_b64 s[68:69], vcc
	s_xor_b64 s[68:69], exec, s[68:69]
	s_cbranch_execz .Lm3b_3_2703
	v_and_b32_e32 v198, 0xfffffc00, v6
	s_movk_i32 s70, 0x400
	v_cmp_ne_u32_e32 vcc, s70, v198
	v_or_b32_e32 v205, s64, v202
	v_mov_b32_e32 v204, s65
	s_and_saveexec_b64 s[70:71], vcc
	s_xor_b64 s[70:71], exec, s[70:71]
	v_mov_b64_e32 v[198:199], s[34:35]
	v_mad_u64_u32 v[198:199], s[80:81], v205, s33, v[198:199]
	v_mov_b32_e32 v200, v199
	v_mad_u64_u32 v[200:201], s[80:81], v204, s33, v[200:201]
	v_mov_b32_e32 v199, v200
	s_mov_b64 s[80:81], 0x3000
	v_lshl_add_u64 v[198:199], v[198:199], 0, s[80:81]
	s_or_saveexec_b64 s[70:71], s[70:71]
	v_mov_b32_e32 v200, 0x130
	v_mov_b32_e32 v201, v69
	s_xor_b64 exec, exec, s[70:71]
	v_mov_b64_e32 v[198:199], s[36:37]
	v_mad_u64_u32 v[198:199], s[80:81], v205, s72, v[198:199]
	v_mov_b32_e32 v200, v199
	v_mad_u64_u32 v[200:201], s[80:81], v204, s72, v[200:201]
	v_mov_b32_e32 v199, v200
	v_lshl_add_u64 v[198:199], v[198:199], 0, s[56:57]
	v_mov_b32_e32 v200, 0x110
	v_mov_b32_e32 v201, v70
	s_or_b64 exec, exec, s[70:71]
.Lm3b_3_2703:
	s_andn2_saveexec_b64 s[68:69], s[68:69]
	s_cbranch_execz .Lm3b_t3
	v_lshrrev_b32_e32 v198, 4, v6
	v_or_b32_e32 v200, s64, v198
	v_mov_b64_e32 v[198:199], s[36:37]
	s_mul_i32 s80, s65, 0x1400
	v_mad_u64_u32 v[198:199], s[70:71], v200, s72, v[198:199]
	v_add_u32_e32 v199, s80, v199
	v_lshl_add_u64 v[198:199], v[198:199], 0, s[58:59]
	v_mov_b32_e32 v200, 0x110
	v_mov_b32_e32 v201, v52
	s_branch .Lm3b_t3
.Lm3b_t3:
	s_or_b64 exec, exec, s[68:69]
	v_lshl_add_u64 v[198:199], v[198:199], 0, s[0:1]
	v_lshl_add_u64 v[198:199], v[198:199], 0, v[50:51]
	global_load_dwordx4 v[204:207], v[198:199], off
	v_mad_u32_u24 v198, v200, v202, v201
	v_add_u32_e32 v6, 0x200, v6
	s_movk_i32 s68, 0x3ff
	v_bfe_u32 v218, v6, 4, 6
	v_cmp_lt_u32_e32 vcc, s68, v6
	s_and_saveexec_b64 s[68:69], vcc
	s_xor_b64 s[68:69], exec, s[68:69]
	s_cbranch_execz .Lm3b_4_2703
	v_and_b32_e32 v214, 0xfffffc00, v6
	s_movk_i32 s70, 0x400
	v_cmp_ne_u32_e32 vcc, s70, v214
	v_or_b32_e32 v221, s64, v218
	v_mov_b32_e32 v220, s65
	s_and_saveexec_b64 s[70:71], vcc
	s_xor_b64 s[70:71], exec, s[70:71]
	v_mov_b64_e32 v[214:215], s[34:35]
	v_mad_u64_u32 v[214:215], s[80:81], v221, s33, v[214:215]
	v_mov_b32_e32 v216, v215
	v_mad_u64_u32 v[216:217], s[80:81], v220, s33, v[216:217]
	v_mov_b32_e32 v215, v216
	s_mov_b64 s[80:81], 0x3000
	v_lshl_add_u64 v[214:215], v[214:215], 0, s[80:81]
	s_or_saveexec_b64 s[70:71], s[70:71]
	v_mov_b32_e32 v216, 0x130
	v_mov_b32_e32 v217, v69
	s_xor_b64 exec, exec, s[70:71]
	v_mov_b64_e32 v[214:215], s[36:37]
	v_mad_u64_u32 v[214:215], s[80:81], v221, s72, v[214:215]
	v_mov_b32_e32 v216, v215
	v_mad_u64_u32 v[216:217], s[80:81], v220, s72, v[216:217]
	v_mov_b32_e32 v215, v216
	v_lshl_add_u64 v[214:215], v[214:215], 0, s[56:57]
	v_mov_b32_e32 v216, 0x110
	v_mov_b32_e32 v217, v70
	s_or_b64 exec, exec, s[70:71]
.Lm3b_4_2703:
	s_andn2_saveexec_b64 s[68:69], s[68:69]
	s_cbranch_execz .Lm3b_t4
	v_lshrrev_b32_e32 v214, 4, v6
	v_or_b32_e32 v216, s64, v214
	v_mov_b64_e32 v[214:215], s[36:37]
	s_mul_i32 s80, s65, 0x1400
	v_mad_u64_u32 v[214:215], s[70:71], v216, s72, v[214:215]
	v_add_u32_e32 v215, s80, v215
	v_lshl_add_u64 v[214:215], v[214:215], 0, s[58:59]
	v_mov_b32_e32 v216, 0x110
	v_mov_b32_e32 v217, v52
	s_branch .Lm3b_t4
.Lm3b_t4:
	s_or_b64 exec, exec, s[68:69]
	v_lshl_add_u64 v[214:215], v[214:215], 0, s[0:1]
	v_lshl_add_u64 v[214:215], v[214:215], 0, v[50:51]
	global_load_dwordx4 v[220:223], v[214:215], off
	v_mad_u32_u24 v214, v216, v218, v217
	v_add_u32_e32 v6, 0x200, v6
	s_movk_i32 s68, 0x3ff
	v_bfe_u32 v234, v6, 4, 6
	v_cmp_lt_u32_e32 vcc, s68, v6
	s_and_saveexec_b64 s[68:69], vcc
	s_xor_b64 s[68:69], exec, s[68:69]
	s_cbranch_execz .Lm3b_5_2703
	v_and_b32_e32 v230, 0xfffffc00, v6
	s_movk_i32 s70, 0x400
	v_cmp_ne_u32_e32 vcc, s70, v230
	v_or_b32_e32 v237, s64, v234
	v_mov_b32_e32 v236, s65
	s_and_saveexec_b64 s[70:71], vcc
	s_xor_b64 s[70:71], exec, s[70:71]
	v_mov_b64_e32 v[230:231], s[34:35]
	v_mad_u64_u32 v[230:231], s[80:81], v237, s33, v[230:231]
	v_mov_b32_e32 v232, v231
	v_mad_u64_u32 v[232:233], s[80:81], v236, s33, v[232:233]
	v_mov_b32_e32 v231, v232
	s_mov_b64 s[80:81], 0x3000
	v_lshl_add_u64 v[230:231], v[230:231], 0, s[80:81]
	s_or_saveexec_b64 s[70:71], s[70:71]
	v_mov_b32_e32 v232, 0x130
	v_mov_b32_e32 v233, v69
	s_xor_b64 exec, exec, s[70:71]
	v_mov_b64_e32 v[230:231], s[36:37]
	v_mad_u64_u32 v[230:231], s[80:81], v237, s72, v[230:231]
	v_mov_b32_e32 v232, v231
	v_mad_u64_u32 v[232:233], s[80:81], v236, s72, v[232:233]
	v_mov_b32_e32 v231, v232
	v_lshl_add_u64 v[230:231], v[230:231], 0, s[56:57]
	v_mov_b32_e32 v232, 0x110
	v_mov_b32_e32 v233, v70
	s_or_b64 exec, exec, s[70:71]
.Lm3b_5_2703:
	s_andn2_saveexec_b64 s[68:69], s[68:69]
	s_cbranch_execz .Lm3b_t5
	v_lshrrev_b32_e32 v230, 4, v6
	v_or_b32_e32 v232, s64, v230
	v_mov_b64_e32 v[230:231], s[36:37]
	s_mul_i32 s80, s65, 0x1400
	v_mad_u64_u32 v[230:231], s[70:71], v232, s72, v[230:231]
	v_add_u32_e32 v231, s80, v231
	v_lshl_add_u64 v[230:231], v[230:231], 0, s[58:59]
	v_mov_b32_e32 v232, 0x110
	v_mov_b32_e32 v233, v52
	s_branch .Lm3b_t5
.Lm3b_t5:
	s_or_b64 exec, exec, s[68:69]
	v_lshl_add_u64 v[230:231], v[230:231], 0, s[0:1]
	v_lshl_add_u64 v[230:231], v[230:231], 0, v[50:51]
	global_load_dwordx4 v[236:239], v[230:231], off
	v_mad_u32_u24 v230, v232, v234, v233
	s_waitcnt vmcnt(5)
	ds_write_b128 v150, v[156:159]
	s_waitcnt vmcnt(4)
	ds_write_b128 v166, v[172:175]
	s_waitcnt vmcnt(3)
	ds_write_b128 v182, v[188:191]
	s_waitcnt vmcnt(2)
	ds_write_b128 v198, v[204:207]
	s_waitcnt vmcnt(1)
	ds_write_b128 v214, v[220:223]
	s_waitcnt vmcnt(0)
	ds_write_b128 v230, v[236:239]

; #define LAS __attribute__((address_space(3)))
; DI void ml3_unit(const Params& P, const Frame& F, int L, int cidx) {
;     ...
;     for (int id = F.tid; id < 2304; id += NTHR) { const int row = id >> 4, ch = id & 15; *(LAS u32x4*)(Cs + row * 272 + ch * 16) = *(const u32x4*)(CST + row * 128 + ch * 8); }
.LBB0_2709:
	v_add_u32_e32 v222, 0x800, v6
	s_movk_i32 s0, 0x8ff
	v_cmp_ge_i32_e32 vcc, s0, v222
	s_mov_b64 s[66:67], exec
	s_and_b64 exec, exec, vcc
	v_ashrrev_i32_e32 v214, 4, v222
	v_lshlrev_b32_e32 v216, 7, v214
	v_ashrrev_i32_e32 v217, 31, v216
	v_lshl_add_u64 v[216:217], v[216:217], 1, v[4:5]
	v_mad_u64_u32 v[220:221], s[68:69], v214, s3, v[52:53]
	global_load_dwordx4 v[216:219], v[216:217], off
	s_mov_b64 exec, s[66:67]
	v_ashrrev_i32_e32 v150, 4, v6
	v_lshlrev_b32_e32 v152, 7, v150
	v_ashrrev_i32_e32 v153, 31, v152
	v_lshl_add_u64 v[152:153], v[152:153], 1, v[4:5]
	v_mad_u64_u32 v[156:157], s[68:69], v150, s3, v[52:53]
	global_load_dwordx4 v[152:155], v[152:153], off
	v_add_u32_e32 v6, 0x200, v6
	v_ashrrev_i32_e32 v166, 4, v6
	v_lshlrev_b32_e32 v168, 7, v166
	v_ashrrev_i32_e32 v169, 31, v168
	v_lshl_add_u64 v[168:169], v[168:169], 1, v[4:5]
	v_mad_u64_u32 v[172:173], s[68:69], v166, s3, v[52:53]
	global_load_dwordx4 v[168:171], v[168:169], off
	v_add_u32_e32 v6, 0x200, v6
	v_ashrrev_i32_e32 v182, 4, v6
	v_lshlrev_b32_e32 v184, 7, v182
	v_ashrrev_i32_e32 v185, 31, v184
	v_lshl_add_u64 v[184:185], v[184:185], 1, v[4:5]
	v_mad_u64_u32 v[188:189], s[68:69], v182, s3, v[52:53]
	global_load_dwordx4 v[184:187], v[184:185], off
	v_add_u32_e32 v6, 0x200, v6
	v_ashrrev_i32_e32 v198, 4, v6
	v_lshlrev_b32_e32 v200, 7, v198
	v_ashrrev_i32_e32 v201, 31, v200
	v_lshl_add_u64 v[200:201], v[200:201], 1, v[4:5]
	v_mad_u64_u32 v[204:205], s[68:69], v198, s3, v[52:53]
	global_load_dwordx4 v[200:203], v[200:201], off
	s_waitcnt vmcnt(3)
	ds_write_b128 v156, v[152:155] offset:54272
	s_waitcnt vmcnt(2)
	ds_write_b128 v172, v[168:171] offset:54272
	s_waitcnt vmcnt(1)
	ds_write_b128 v188, v[184:187] offset:54272
	s_waitcnt vmcnt(0)
	ds_write_b128 v204, v[200:203] offset:54272
	v_cmp_ge_i32_e32 vcc, s0, v222
	s_mov_b64 s[66:67], exec
	s_and_b64 exec, exec, vcc
	s_waitcnt vmcnt(0)
	ds_write_b128 v220, v[216:219] offset:54272
	s_mov_b64 exec, s[66:67]

.LBB0_2782:
	s_cmp_lt_u32 s3, 0x40001
	s_mov_b64 s[18:19], 0
	s_cselect_b64 s[20:21], -1, 0
	s_mov_b64 s[22:23], -1
	s_and_b64 vcc, exec, s[20:21]
	s_cbranch_vccnz .LBB0_2779
	s_branch .LBB0_2776
	s_nop 0
	s_nop 0
	s_nop 0
	s_nop 0
	s_nop 0
	s_nop 0
	s_nop 0
	s_nop 0
	s_nop 0
	s_nop 0
	s_nop 0
	s_nop 0
	s_nop 0
	s_nop 0
	s_nop 0
	s_nop 0
	s_nop 0
	s_nop 0
	s_nop 0
	s_nop 0
	s_nop 0
	s_nop 0
	s_nop 0
	s_nop 0
	s_nop 0
	s_nop 0
	s_nop 0
